# hoist1
# speedup vs baseline: 1.0608x; 1.0213x over previous
_Z10gae_kernelPKfPKiS2_S0_S0_S0_PfS3_:
	s_load_dwordx8 s[4:11], s[0:1], 0x0
	s_load_dwordx4 s[12:15], s[0:1], 0x20
	s_load_dwordx4 s[20:23], s[0:1], 0x30
	v_and_b32_e32 v64, 63, v0
	v_lshrrev_b32_e32 v1, 6, v0
	s_andn2_b32 s16, s2, 63
	s_and_b32 s17, s2, 7
	s_lshl_b32 s17, s17, 3
	s_bfe_u32 s18, s2, 0x30003
	s_or_b32 s16, s16, s17
	s_or_b32 s2, s16, s18
	s_mov_b32 s3, 0
	s_lshl_b64 s[2:3], s[2:3], 11
	v_lshlrev_b32_e32 v2, 9, v1
	v_lshlrev_b32_e32 v3, 2, v64
	v_or3_b32 v2, s2, v2, v3
	v_mov_b32_e32 v3, s3
	v_lshlrev_b64 v[18:19], 2, v[2:3]
	s_waitcnt lgkmcnt(0)
	v_lshl_add_u64 v[54:55], s[14:15], 0, v[18:19]
	v_lshl_add_u64 v[52:53], s[6:7], 0, v[18:19]
	global_load_dwordx4 v[10:13], v[54:55], off sc0 sc1 nt
	global_load_dwordx4 v[14:17], v[52:53], off sc0 sc1 nt
	v_lshl_add_u64 v[56:57], s[8:9], 0, v[18:19]
	global_load_dwordx4 v[20:23], v[56:57], off sc0 sc1 nt
	v_lshl_add_u64 v[58:59], s[12:13], 0, v[18:19]
	global_load_dwordx4 v[24:27], v[58:59], off sc0 sc1 nt
	v_lshl_add_u64 v[60:61], s[4:5], 0, v[18:19]
	global_load_dwordx4 v[28:31], v[60:61], off sc0 sc1 nt
	v_lshl_add_u64 v[62:63], s[10:11], 0, v[18:19]
	global_load_dwordx4 v[2:5], v[62:63], off sc0 sc1 nt
	global_load_dwordx4 v[32:35], v[60:61], off offset:1024 sc0 sc1 nt
	global_load_dwordx4 v[36:39], v[52:53], off offset:1024 sc0 sc1 nt
	global_load_dwordx4 v[40:43], v[56:57], off offset:1024 sc0 sc1 nt
	global_load_dwordx4 v[6:9], v[62:63], off offset:1024 sc0 sc1 nt
	global_load_dwordx4 v[44:47], v[58:59], off offset:1024 sc0 sc1 nt
	global_load_dwordx4 v[48:51], v[54:55], off offset:1024 sc0 sc1 nt
	v_mov_b32_e32 v66, 0
	v_mov_b32_e32 v68, 1.0
	v_mov_b32_e32 v69, 0
	v_mov_b32_e32 v70, 1.0
	v_mov_b32_e32 v71, 0
	v_mov_b32_e32 v72, 1.0
	v_bfe_u32 v73, v0, 4, 2
	v_cmp_gt_u32_e64 s[4:5], 16, v64
	v_mov_b32_e32 v65, 0
	v_mov_b32_e32 v67, 1.0
	s_waitcnt vmcnt(11)
	v_mul_f32_e32 v12, 0x3f7d70a4, v12
	s_waitcnt vmcnt(10)
	v_cmp_eq_u32_e32 vcc, 0, v14
	v_mul_f32_e32 v13, 0x3f7d70a4, v13
	v_mul_f32_e32 v10, 0x3f7d70a4, v10
	v_cndmask_b32_e64 v14, 0, 1.0, vcc
	s_waitcnt vmcnt(9)
	v_cmp_eq_u32_e32 vcc, 0, v20
	v_mul_f32_e32 v11, 0x3f7d70a4, v11
	s_waitcnt vmcnt(8)
	v_mul_f32_e32 v26, v26, v12
	v_cndmask_b32_e64 v20, 0, 1.0, vcc
	v_cmp_eq_u32_e32 vcc, 0, v15
	v_mul_f32_e32 v27, v27, v13
	v_mul_f32_e32 v24, v24, v10
	v_cndmask_b32_e64 v15, 0, 1.0, vcc
	v_cmp_eq_u32_e32 vcc, 0, v21
	v_mul_f32_e32 v25, v25, v11
	v_mul_f32_e32 v12, 0x3f733333, v12
	v_cndmask_b32_e64 v21, 0, 1.0, vcc
	v_cmp_eq_u32_e32 vcc, 0, v16
	v_mul_f32_e32 v13, 0x3f733333, v13
	v_mul_f32_e32 v10, 0x3f733333, v10
	v_cndmask_b32_e64 v16, 0, 1.0, vcc
	v_cmp_eq_u32_e32 vcc, 0, v22
	s_waitcnt vmcnt(7)
	v_fma_f32 v16, v26, v16, v30
	v_mul_f32_e32 v11, 0x3f733333, v11
	v_cndmask_b32_e64 v22, 0, 1.0, vcc
	v_cmp_eq_u32_e32 vcc, 0, v17
	v_fma_f32 v14, v24, v14, v28
	v_fma_f32 v15, v25, v15, v29
	v_cndmask_b32_e64 v17, 0, 1.0, vcc
	v_cmp_eq_u32_e32 vcc, 0, v23
	v_fmac_f32_e32 v31, v27, v17
	v_mul_f32_e32 v22, v12, v22
	v_cndmask_b32_e64 v23, 0, 1.0, vcc
	v_mul_f32_e32 v23, v13, v23
	s_waitcnt vmcnt(6)
	v_sub_f32_e32 v12, v16, v4
	v_sub_f32_e32 v13, v31, v5
	v_mul_f32_e32 v20, v10, v20
	v_mul_f32_e32 v21, v11, v21
	v_sub_f32_e32 v10, v14, v2
	v_sub_f32_e32 v11, v15, v3
	v_mul_f32_e32 v14, v23, v22
	v_fma_f32 v15, v22, v13, v12
	v_mul_f32_e32 v14, v14, v21
	v_fma_f32 v15, v21, v15, v11
	v_mul_f32_e32 v14, v14, v20
	v_fma_f32 v24, v20, v15, v10
	v_mov_b32_e32 v16, 1.0
	v_mov_b32_dpp v68, v14 row_shl:1 row_mask:0xf bank_mask:0xf
	v_mov_b32_dpp v66, v24 row_shl:1 row_mask:0xf bank_mask:0xf
	v_mul_f32_e32 v15, v14, v68
	v_fmac_f32_e32 v24, v14, v66
	v_cmp_eq_u32_e32 vcc, 2, v73
	v_mov_b32_dpp v70, v15 row_shl:2 row_mask:0xf bank_mask:0xf
	v_mov_b32_dpp v69, v24 row_shl:2 row_mask:0xf bank_mask:0xf
	v_mul_f32_e32 v14, v15, v70
	v_fmac_f32_e32 v24, v15, v69
	v_mov_b32_e32 v15, 0
	v_mov_b32_dpp v72, v14 row_shl:4 row_mask:0xf bank_mask:0xf
	v_mov_b32_dpp v71, v24 row_shl:4 row_mask:0xf bank_mask:0xf
	v_fmac_f32_e32 v24, v14, v71
	v_mul_f32_e32 v14, v14, v72
	s_nop 0
	v_mov_b32_dpp v15, v24 row_shl:8 row_mask:0xf bank_mask:0xf
	v_mov_b32_dpp v16, v14 row_shl:8 row_mask:0xf bank_mask:0xf
	v_fmac_f32_e32 v24, v14, v15
	v_mul_f32_e32 v14, v14, v16
	v_readlane_b32 s9, v24, 32
	v_readlane_b32 s2, v14, 48
	v_readlane_b32 s8, v14, 32
	v_readlane_b32 s6, v14, 16
	v_mov_b32_e32 v15, s2
	v_mul_f32_e32 v16, s8, v15
	v_cndmask_b32_e32 v15, 1.0, v15, vcc
	v_cmp_eq_u32_e64 s[2:3], 1, v73
	v_readlane_b32 s10, v24, 48
	v_mul_f32_e32 v17, s6, v16
	v_cndmask_b32_e64 v15, v15, v16, s[2:3]
	v_readlane_b32 s7, v24, 16
	v_cndmask_b32_e64 v15, v15, v17, s[4:5]
	v_mov_b32_e32 v16, s9
	v_mov_b32_e32 v17, s10
	v_fmac_f32_e32 v16, s8, v17
	v_mov_b32_e32 v25, s7
	v_cndmask_b32_e32 v17, 0, v17, vcc
	v_fmac_f32_e32 v25, s6, v16
	v_cndmask_b32_e64 v16, v17, v16, s[2:3]
	v_cndmask_b32_e64 v16, v16, v25, s[4:5]
	s_waitcnt vmcnt(4)
	v_cmp_eq_u32_e64 s[6:7], 0, v36
	v_fmac_f32_e32 v24, v14, v16
	v_mul_f32_e32 v28, v14, v15
	s_waitcnt vmcnt(0)
	v_mul_f32_e32 v15, 0x3f7d70a4, v48
	v_cndmask_b32_e64 v14, 0, 1.0, s[6:7]
	v_cmp_eq_u32_e64 s[6:7], 0, v40
	v_mul_f32_e32 v17, v44, v15
	v_mul_f32_e32 v15, 0x3f733333, v15
	v_cndmask_b32_e64 v16, 0, 1.0, s[6:7]
	v_cmp_eq_u32_e64 s[6:7], 0, v37
	v_mul_f32_e32 v25, v15, v16
	v_mul_f32_e32 v16, 0x3f7d70a4, v49
	v_cndmask_b32_e64 v15, 0, 1.0, s[6:7]
	v_cmp_eq_u32_e64 s[6:7], 0, v41
	v_fma_f32 v14, v17, v14, v32
	v_mul_f32_e32 v26, v45, v16
	v_cndmask_b32_e64 v17, 0, 1.0, s[6:7]
	v_mul_f32_e32 v16, 0x3f733333, v16
	v_fma_f32 v15, v26, v15, v33
	v_mul_f32_e32 v26, v16, v17
	v_mul_f32_e32 v17, 0x3f7d70a4, v50
	v_cmp_eq_u32_e64 s[6:7], 0, v38
	v_mul_f32_e32 v29, v46, v17
	v_mul_f32_e32 v17, 0x3f733333, v17
	v_cndmask_b32_e64 v16, 0, 1.0, s[6:7]
	v_cmp_eq_u32_e64 s[6:7], 0, v42
	v_fma_f32 v16, v29, v16, v34
	v_mul_f32_e32 v29, 0x3f7d70a4, v51
	v_cndmask_b32_e64 v27, 0, 1.0, s[6:7]
	v_cmp_eq_u32_e64 s[6:7], 0, v39
	v_mul_f32_e32 v27, v17, v27
	v_mul_f32_e32 v31, v47, v29
	v_cndmask_b32_e64 v17, 0, 1.0, s[6:7]
	v_cmp_eq_u32_e64 s[6:7], 0, v43
	v_fmac_f32_e32 v35, v31, v17
	v_mul_f32_e32 v29, 0x3f733333, v29
	v_cndmask_b32_e64 v30, 0, 1.0, s[6:7]
	v_sub_f32_e32 v16, v16, v8
	v_sub_f32_e32 v17, v35, v9
	v_mul_f32_e32 v29, v29, v30
	v_sub_f32_e32 v15, v15, v7
	v_fma_f32 v30, v27, v17, v16
	v_mul_f32_e32 v31, v29, v27
	v_sub_f32_e32 v14, v14, v6
	v_fma_f32 v30, v26, v30, v15
	v_mul_f32_e32 v31, v31, v26
	v_fma_f32 v30, v25, v30, v14
	v_mul_f32_e32 v31, v31, v25
	v_mov_b32_e32 v32, 0
	v_mov_b32_e32 v33, 1.0
	s_nop 0
	v_mov_b32_dpp v32, v30 row_shl:1 row_mask:0xf bank_mask:0xf
	v_mov_b32_dpp v33, v31 row_shl:1 row_mask:0xf bank_mask:0xf
	v_fmac_f32_e32 v30, v31, v32
	v_mul_f32_e32 v31, v31, v33
	v_mov_b32_e32 v32, 0
	v_mov_b32_e32 v33, 1.0
	s_nop 0
	v_mov_b32_dpp v32, v30 row_shl:2 row_mask:0xf bank_mask:0xf
	v_mov_b32_dpp v33, v31 row_shl:2 row_mask:0xf bank_mask:0xf
	v_fmac_f32_e32 v30, v31, v32
	v_mul_f32_e32 v31, v31, v33
	v_mov_b32_e32 v32, 0
	v_mov_b32_e32 v33, 1.0
	s_nop 0
	v_mov_b32_dpp v32, v30 row_shl:4 row_mask:0xf bank_mask:0xf
	v_mov_b32_dpp v33, v31 row_shl:4 row_mask:0xf bank_mask:0xf
	v_fmac_f32_e32 v30, v31, v32
	v_mul_f32_e32 v31, v31, v33
	s_nop 0
	v_mov_b32_dpp v65, v30 row_shl:8 row_mask:0xf bank_mask:0xf
	v_mov_b32_dpp v67, v31 row_shl:8 row_mask:0xf bank_mask:0xf
	v_fmac_f32_e32 v30, v31, v65
	v_mul_f32_e32 v31, v31, v67
	v_readlane_b32 s9, v30, 32
	v_readlane_b32 s10, v31, 48
	v_readlane_b32 s8, v31, 32
	v_readlane_b32 s6, v31, 16
	v_mov_b32_e32 v32, s10
	v_mul_f32_e32 v33, s8, v32
	v_cndmask_b32_e32 v32, 1.0, v32, vcc
	v_readlane_b32 s11, v30, 48
	v_mul_f32_e32 v34, s6, v33
	v_cndmask_b32_e64 v32, v32, v33, s[2:3]
	v_readlane_b32 s7, v30, 16
	v_cndmask_b32_e64 v32, v32, v34, s[4:5]
	v_mov_b32_e32 v33, s9
	v_mov_b32_e32 v34, s11
	v_fmac_f32_e32 v33, s8, v34
	v_mov_b32_e32 v35, s7
	v_cndmask_b32_e32 v34, 0, v34, vcc
	v_fmac_f32_e32 v35, s6, v33
	v_cndmask_b32_e64 v33, v34, v33, s[2:3]
	v_cndmask_b32_e64 v33, v33, v35, s[4:5]
	v_fmac_f32_e32 v30, v31, v33
	v_mul_f32_e32 v31, v31, v32
	v_readlane_b32 s6, v28, 0
	v_readlane_b32 s7, v24, 0
	v_readlane_b32 s4, v31, 0
	v_readlane_b32 s5, v30, 0
	v_cmp_eq_u32_e32 vcc, 0, v64
	s_and_saveexec_b64 s[2:3], vcc
	s_cbranch_execz .LBB0_4
	v_mov_b32_e32 v32, s4
	v_mov_b32_e32 v33, s7
	v_mov_b32_e32 v34, s5
	v_mul_f32_e32 v32, s6, v32
	v_lshlrev_b32_e32 v1, 2, v1
	v_fmac_f32_e32 v33, s6, v34
	ds_write2_b32 v1, v32, v33 offset1:4
.LBB0_4:
	s_or_b64 exec, exec, s[2:3]
	v_mov_b32_e32 v1, 0
	s_waitcnt lgkmcnt(0)
	s_barrier
	ds_read2_b32 v[32:33], v1 offset0:3 offset1:7
	ds_read2_b32 v[34:35], v1 offset0:1 offset1:2
	ds_read2_b32 v[36:37], v1 offset0:5 offset1:6
	s_movk_i32 s6, 0xc0
	v_cmp_gt_u32_e32 vcc, s6, v0
	s_movk_i32 s6, 0x80
	s_waitcnt lgkmcnt(2)
	v_fmac_f32_e32 v33, 0, v32
	v_cndmask_b32_e32 v1, 0, v33, vcc
	s_waitcnt lgkmcnt(0)
	v_fma_f32 v32, v35, v1, v37
	v_cmp_gt_u32_e32 vcc, s6, v0
	s_nop 1
	v_cndmask_b32_e32 v1, v1, v32, vcc
	v_fmac_f32_e32 v36, v34, v1
	v_cmp_gt_u32_e32 vcc, 64, v0
	s_nop 1
	v_cndmask_b32_e32 v0, v1, v36, vcc
	v_mov_b32_e32 v1, s5
	v_fmac_f32_e32 v1, s4, v0
	v_fmac_f32_e32 v24, v28, v1
	v_fmac_f32_e32 v30, v31, v0
	s_nop 0
	v_mov_b32_dpp v1, v24 wave_shl:1 row_mask:0xf bank_mask:0xf
	v_fmac_f32_e32 v13, v23, v1
	v_mov_b32_dpp v0, v30 wave_shl:1 row_mask:0xf bank_mask:0xf
	v_fmac_f32_e32 v12, v22, v13
	v_fmac_f32_e32 v17, v29, v0
	v_fmac_f32_e32 v11, v21, v12
	v_fmac_f32_e32 v16, v27, v17
	v_fmac_f32_e32 v10, v20, v11
	s_waitcnt lgkmcnt(0)
	v_lshl_add_u64 v[20:21], s[20:21], 0, v[18:19]
	v_fmac_f32_e32 v15, v26, v16
	v_pk_add_f32 v[4:5], v[12:13], v[4:5]
	v_pk_add_f32 v[2:3], v[10:11], v[2:3]
	global_store_dwordx4 v[20:21], v[10:13], off sc1 nt
	v_fmac_f32_e32 v14, v25, v15
	v_pk_add_f32 v[0:1], v[14:15], v[6:7]
	v_lshl_add_u64 v[10:11], s[22:23], 0, v[18:19]
	global_store_dwordx4 v[10:11], v[2:5], off sc1 nt
	s_nop 1
	v_pk_add_f32 v[2:3], v[16:17], v[8:9]
	global_store_dwordx4 v[20:21], v[14:17], off offset:1024 sc1 nt
	global_store_dwordx4 v[10:11], v[0:3], off offset:1024 sc1 nt
	s_endpgm
